# baseline (speedup 1.0000x reference)
_Z10snn_kernel6Params:
	s_load_dwordx16 s[44:59], s[0:1], 0x0
	s_load_dwordx8 s[60:67], s[0:1], 0x40
	v_and_b32_e32 v98, 0x3ff, v0
	s_lshr_b32 s33, s2, 3
	v_lshlrev_b32_e32 v1, 2, v98
	s_lshl_b32 s3, s33, 4
	v_and_b32_e32 v107, 12, v1
	v_bfe_u32 v109, v0, 2, 8
	v_or_b32_e32 v1, s3, v107
	s_waitcnt lgkmcnt(0)
	v_bfe_u32 v252, v0, 4, 4
	v_or_b32_e32 v252, s3, v252
	s_and_b32 s82, s2, 7
	s_lshl_b32 s82, s82, 9
	v_add_u32_e32 v253, s82, v252
	v_lshlrev_b32_e32 v252, 2, v252
	v_lshlrev_b32_e32 v253, 2, v253
	v_and_b32_e32 v161, 0xff, v0
	v_lshlrev_b32_e32 v161, 2, v161
	global_load_dword v252, v252, s[56:57]
	global_load_dword v253, v253, s[58:59]
	global_load_dword v162, v161, s[50:51] offset:1024
	global_load_dword v161, v161, s[50:51]
	s_add_u32 s4, s62, 0x100000
	v_lshl_add_u32 v100, v109, 9, v1
	v_mov_b32_e32 v101, 0
	s_addc_u32 s5, s63, 0
	v_lshlrev_b64 v[2:3], 2, v[100:101]
	s_add_u32 s6, s62, 0x200000
	v_lshl_add_u64 v[4:5], s[46:47], 0, v[2:3]
	s_addc_u32 s7, s63, 0
	global_load_dwordx4 v[94:97], v[4:5], off
	v_lshl_add_u64 v[4:5], s[62:63], 0, v[2:3]
	v_lshl_add_u64 v[6:7], s[4:5], 0, v[2:3]
	global_load_dwordx4 v[90:93], v[4:5], off
	global_load_dwordx4 v[86:89], v[6:7], off
	v_lshl_add_u64 v[4:5], s[6:7], 0, v[2:3]
	v_or_b32_e32 v105, 0x80, v109
	global_load_dwordx4 v[82:85], v[4:5], off
	v_lshl_add_u64 v[4:5], s[52:53], 0, v[2:3]
	v_lshl_add_u64 v[2:3], s[54:55], 0, v[2:3]
	v_lshl_add_u32 v100, v105, 9, v1
	global_load_dwordx4 v[78:81], v[2:3], off
	v_lshlrev_b64 v[2:3], 2, v[100:101]
	global_load_dwordx4 v[74:77], v[4:5], off
	v_lshl_add_u64 v[4:5], s[46:47], 0, v[2:3]
	global_load_dwordx4 v[70:73], v[4:5], off
	v_lshl_add_u64 v[4:5], s[62:63], 0, v[2:3]
	v_lshl_add_u64 v[6:7], s[4:5], 0, v[2:3]
	global_load_dwordx4 v[66:69], v[4:5], off
	global_load_dwordx4 v[62:65], v[6:7], off
	v_lshl_add_u64 v[4:5], s[6:7], 0, v[2:3]
	v_or_b32_e32 v103, 0x100, v109
	global_load_dwordx4 v[58:61], v[4:5], off
	v_lshl_add_u64 v[4:5], s[52:53], 0, v[2:3]
	v_lshl_add_u64 v[2:3], s[54:55], 0, v[2:3]
	v_lshl_add_u32 v100, v103, 9, v1
	global_load_dwordx4 v[54:57], v[2:3], off
	v_lshlrev_b64 v[2:3], 2, v[100:101]
	global_load_dwordx4 v[50:53], v[4:5], off
	v_lshl_add_u64 v[4:5], s[46:47], 0, v[2:3]
	global_load_dwordx4 v[46:49], v[4:5], off
	v_lshl_add_u64 v[4:5], s[62:63], 0, v[2:3]
	v_or_b32_e32 v99, 0x180, v109
	v_lshl_add_u64 v[6:7], s[4:5], 0, v[2:3]
	global_load_dwordx4 v[42:45], v[4:5], off
	global_load_dwordx4 v[38:41], v[6:7], off
	v_lshl_add_u64 v[4:5], s[6:7], 0, v[2:3]
	v_lshl_add_u32 v100, v99, 9, v1
	global_load_dwordx4 v[34:37], v[4:5], off
	v_lshl_add_u64 v[4:5], s[52:53], 0, v[2:3]
	v_lshl_add_u64 v[2:3], s[54:55], 0, v[2:3]
	v_lshlrev_b64 v[6:7], 2, v[100:101]
	v_and_b32_e32 v8, 0x1fc, v0
	global_load_dwordx4 v[30:33], v[2:3], off
	v_lshl_add_u64 v[2:3], s[46:47], 0, v[6:7]
	global_load_dwordx4 v[26:29], v[4:5], off
	global_load_dword v108, v8, s[60:61]
	global_load_dword v106, v8, s[60:61] offset:512
	global_load_dword v104, v8, s[60:61] offset:1024
	global_load_dword v102, v8, s[60:61] offset:1536
	global_load_dwordx4 v[22:25], v[2:3], off
	v_lshl_add_u64 v[2:3], s[62:63], 0, v[6:7]
	v_lshl_add_u64 v[4:5], s[4:5], 0, v[6:7]
	global_load_dwordx4 v[10:13], v[2:3], off
	global_load_dwordx4 v[18:21], v[4:5], off
	v_lshl_add_u64 v[2:3], s[6:7], 0, v[6:7]
	global_load_dwordx4 v[14:17], v[2:3], off
	v_lshl_add_u64 v[2:3], s[52:53], 0, v[6:7]
	v_lshl_add_u64 v[6:7], s[54:55], 0, v[6:7]
	global_load_dwordx4 v[2:5], v[2:3], off
	v_readfirstlane_b32 s76, v98
	global_load_dwordx4 v[6:9], v[6:7], off
	v_cmp_eq_u32_e32 vcc, 0, v98
	s_and_saveexec_b64 s[4:5], vcc
	v_mov_b32_e32 v1, 0x26c00
	ds_write_b32 v1, v101
	s_or_b64 exec, exec, s[4:5]
	v_cmp_gt_u32_e32 vcc, 4, v98
	s_and_saveexec_b64 s[4:5], vcc
	v_mov_b32_e32 v1, 0x26c10
	v_lshl_add_u32 v1, v98, 2, v1
	v_mov_b32_e32 v100, 0
	ds_write_b32 v1, v100
	s_or_b64 exec, exec, s[4:5]
	s_load_dwordx2 s[72:73], s[0:1], 0x60
	s_waitcnt vmcnt(9)
	v_mul_f32_e64 v101, v108, |v94|
	v_cmp_neq_f32_e32 vcc, 0, v101
	s_mov_b64 s[4:5], 0
	s_and_saveexec_b64 s[8:9], vcc
	v_cmp_neq_f32_e64 s[4:5], 0, v90
	v_cmp_neq_f32_e64 s[6:7], 0, v86
	s_or_b64 s[6:7], s[4:5], s[6:7]
	v_cmp_neq_f32_e64 s[4:5], 0, v82
	s_or_b64 s[4:5], s[6:7], s[4:5]
	s_and_b64 s[4:5], s[4:5], exec
	s_or_b64 exec, exec, s[8:9]
	v_mov_b32_e32 v1, 0
	s_and_saveexec_b64 s[6:7], vcc
	v_cmp_neq_f32_e32 vcc, 0, v90
	s_nop 1
	v_cndmask_b32_e64 v1, 0, 1, vcc
	v_cmp_neq_f32_e32 vcc, 0, v86
	s_nop 1
	v_cndmask_b32_e64 v94, 0, 1, vcc
	v_cmp_neq_f32_e32 vcc, 0, v82
	s_nop 1
	v_addc_co_u32_e32 v1, vcc, v94, v1, vcc
	v_cmp_lt_u32_e32 vcc, 1, v1
	s_nop 1
	v_cndmask_b32_e64 v1, 0, 1, vcc
	s_or_b64 exec, exec, s[6:7]
	v_cmp_neq_f32_e32 vcc, 0, v86
	s_nop 1
	v_cndmask_b32_e64 v94, 2, 1, vcc
	v_cmp_eq_f32_e32 vcc, 0, v90
	s_nop 1
	v_cndmask_b32_e32 v110, 0, v94, vcc
	v_cmp_lt_i32_e32 vcc, 0, v110
	s_and_saveexec_b64 s[6:7], vcc
	s_cbranch_execz .LBB0_12
	v_cmp_ne_u32_e32 vcc, 1, v110
	s_and_saveexec_b64 s[8:9], vcc
	s_xor_b64 s[8:9], exec, s[8:9]
	s_andn2_saveexec_b64 s[8:9], s[8:9]
	v_mov_b32_e32 v82, v86
	s_or_b64 exec, exec, s[8:9]
	v_mov_b32_e32 v90, v82

.LBB0_267:
	s_or_b64 exec, exec, s[44:45]
	s_waitcnt lgkmcnt(1)
	v_mov_b32_e32 v0, s56
	v_mov_b32_e32 v1, s57
	v_or_b32_e32 v6, s3, v75
	s_lshl_b32 s24, s75, 9
	v_mov_b32_e32 v7, v34
	v_mov_b32_e32 v2, s58
	v_mov_b32_e32 v3, s59
	v_add_u32_e32 v4, s24, v6
	v_mov_b32_e32 v5, v34
	v_lshl_add_u64 v[0:1], v[6:7], 2, v[0:1]
	v_and_b32_e32 v160, 0xff, v98
	v_lshl_add_u64 v[2:3], v[4:5], 2, v[2:3]
	v_mov_b32_e32 v5, v252
	v_lshlrev_b32_e32 v0, 2, v160
	v_mov_b32_e32 v4, v253
	s_mov_b32 s69, s68
	s_mov_b32 s70, s68
	s_mov_b32 s71, s68
	v_mov_b64_e32 v[10:11], s[68:69]
	v_or_b32_e32 v0, 0xc00, v98
	s_movk_i32 s0, 0xe00
	s_getreg_b32 s11, hwreg(HW_REG_XCC_ID, 0, 4)
	v_mov_b64_e32 v[12:13], s[70:71]
	v_cmp_gt_u32_e32 vcc, s0, v0
	s_waitcnt lgkmcnt(0)
	s_barrier
	ds_write_b128 v74, v[10:13]
	ds_write_b128 v74, v[10:13] offset:8192
	ds_write_b128 v74, v[10:13] offset:16384
	ds_write_b128 v74, v[10:13] offset:24576
	ds_write_b128 v74, v[10:13] offset:32768
	ds_write_b128 v74, v[10:13] offset:40960
	ds_write_b128 v74, v[10:13] offset:49152
	s_and_saveexec_b64 s[0:1], vcc
	v_mov_b32_e32 v0, 0
	v_mov_b32_e32 v1, v0
	v_mov_b32_e32 v2, v0
	v_mov_b32_e32 v3, v0
	ds_write_b128 v74, v[0:3] offset:57344
	s_or_b64 exec, exec, s[0:1]
	s_lshr_b32 s10, s76, 6
	s_add_u32 s14, s66, 0x400000
	s_addc_u32 s15, s67, 0
	s_waitcnt lgkmcnt(0)
	s_barrier
	s_and_saveexec_b64 s[0:1], s[42:43]
	s_xor_b64 s[0:1], exec, s[0:1]
	s_lshl_b32 s12, s10, 2
	s_or_saveexec_b64 s[0:1], s[0:1]
	v_mov_b32_e32 v2, 0
	s_and_b32 s68, s11, 15
	v_mov_b32_e32 v3, v2
	v_mov_b32_e32 v163, s12
	s_xor_b64 exec, exec, s[0:1]
	s_cbranch_execz .LBB0_283
	v_mov_b32_e32 v0, 0x24400
	v_lshl_or_b32 v0, v75, 2, v0
	ds_read_b32 v3, v0
	s_waitcnt vmcnt(2)
	v_cvt_f64_f32_e32 v[0:1], v4
	s_lshl_b32 s20, s10, 2
	s_waitcnt lgkmcnt(0)
	v_cvt_f64_f32_e32 v[6:7], v3
	v_add_f64 v[0:1], v[0:1], v[6:7]
	v_cmp_le_f64_e64 s[16:17], 1.0, v[0:1]
	s_lshr_b32 s18, s16, 15
	s_lshr_b64 s[12:13], s[16:17], 30
	s_and_b32 s11, s16, 1
	s_and_b32 s13, s18, 2
	s_and_b32 s12, s12, 4
	s_or_b32 s11, s13, s11
	s_or_b32 s11, s11, s12
	s_lshr_b32 s12, s17, 13
	s_and_b32 s12, s12, 8
	s_or_b32 s11, s11, s12
	s_lshl_b32 s21, s11, s20
	s_and_saveexec_b64 s[10:11], s[4:5]
	s_cbranch_execz .LBB0_276
	s_mov_b64 s[18:19], exec
	v_mbcnt_lo_u32_b32 v2, s18, 0
	v_mbcnt_hi_u32_b32 v2, s19, v2
	s_or_b32 s22, s21, 0x10000
	v_cmp_eq_u32_e32 vcc, 0, v2
	s_and_saveexec_b64 s[12:13], vcc
	s_bcnt1_i32_b64 s18, s[18:19]
	s_mul_i32 s18, s22, s18
	v_mov_b32_e32 v3, 0x26c10
	v_mov_b32_e32 v4, s18
	ds_add_rtn_u32 v3, v3, v4
	s_or_b64 exec, exec, s[12:13]
	s_waitcnt lgkmcnt(0)
	v_readfirstlane_b32 s12, v3
	v_mul_lo_u32 v2, s22, v2
	s_nop 0
	v_add_u32_e32 v2, s12, v2

.LBB0_288:
	s_waitcnt lgkmcnt(0)
	s_barrier
	s_and_saveexec_b64 s[10:11], s[42:43]
	s_xor_b64 s[56:57], exec, s[10:11]
	s_cbranch_execnz .Lmy_rx
.LBB0_304:
	s_andn2_saveexec_b64 s[56:57], s[56:57]
	s_cbranch_execz .LBB0_287
	v_add_u32_e32 v178, 1, v177
	v_lshlrev_b32_e32 v12, 4, v178
	v_cmp_ne_u32_e64 s[10:11], 47, v177
	s_and_b64 vcc, exec, s[6:7]
	v_lshlrev_b32_e32 v181, 12, v177
	v_cndmask_b32_e64 v12, v174, v12, s[10:11]
	v_lshl_add_u32 v12, v12, 2, v169
	ds_read_b32 v179, v12
	s_cbranch_vccz .Lmy_gen

.Lmy_rx:
	v_and_b32_e32 v212, 3, v177
	v_mad_u32_u24 v213, v212, v209, v208
	v_mad_u32_u24 v214, v212, v211, v210
	global_load_dword v182, v213, s[66:67] sc1
	global_load_dword v183, v214, s[66:67] sc1
	v_cmp_eq_u32_e64 s[10:11], 0, v177
	v_cmp_ne_u32_e32 vcc, 0, v177
	s_and_saveexec_b64 s[12:13], vcc
	s_cbranch_execz .LBB0_291
	v_mul_f32_e32 v60, v161, v59
	v_fma_f32 v46, v167, v52, 1.0
	v_mov_b32_e32 v61, v53
	v_pk_mul_f32 v[52:53], v[60:61], v[46:47]
	v_add_u32_e32 v12, -1, v177
	v_pk_fma_f32 v[52:53], v[58:59], s[26:27], v[52:53]
	v_cvt_f64_f32_e32 v[58:59], v59
	v_fmac_f64_e32 v[58:59], s[28:29], v[44:45]
	v_cvt_f64_f32_e32 v[44:45], v57
	v_mul_f32_e32 v62, v162, v57
	v_fma_f32 v50, v168, v50, 1.0
	v_mov_b32_e32 v63, v51
	v_mov_b32_e32 v51, v47
	v_fmac_f64_e32 v[44:45], s[28:29], v[48:49]
	v_cmp_eq_u32_e32 vcc, s33, v12
	v_pk_mul_f32 v[50:51], v[62:63], v[50:51]
	v_mov_b64_e32 v[48:49], v[44:45]
	v_cndmask_b32_e32 v39, v39, v45, vcc
	v_cndmask_b32_e32 v38, v38, v44, vcc
	v_cndmask_b32_e32 v37, v37, v59, vcc
	v_cndmask_b32_e32 v36, v36, v58, vcc
	v_cmp_eq_u32_e32 vcc, s69, v177
	v_pk_fma_f32 v[50:51], v[56:57], s[26:27], v[50:51]
	s_nop 0
	v_cndmask_b32_e32 v5, v5, v45, vcc
	v_cndmask_b32_e32 v4, v4, v44, vcc
	v_cndmask_b32_e32 v7, v7, v59, vcc
	v_cndmask_b32_e32 v6, v6, v58, vcc
	v_mov_b64_e32 v[44:45], v[58:59]

.Lmy_rx_nt0:
	s_mov_b64 s[48:49], s[38:39]
	s_mov_b64 s[50:51], s[40:41]
.Lmy_rx_end:
	s_branch .LBB0_304
.Lmy_gen:
	v_add_u32_e32 v12, 0xf000, v181
	v_add_u32_e32 v46, 0xe000, v181
	v_add_u32_e32 v60, 0xc000, v181
	v_and_or_b32 v182, v60, s3, v171
	v_and_or_b32 v183, v46, s3, v171
	v_and_or_b32 v184, v12, s3, v171
	v_mov_b32_e32 v180, 0
	s_mov_b32 s60, 0
	v_mov_b64_e32 v[60:61], v[42:43]
	v_mov_b64_e32 v[62:63], v[40:41]
	v_mov_b32_e32 v12, v172
	s_branch .LBB0_308

.LBB0_312:
	s_branch .LBB0_318
.LBB0_326:
	s_or_b64 exec, exec, s[24:25]
	s_and_saveexec_b64 s[0:1], s[42:43]
	s_cbranch_execz .LBB0_328
	s_mov_b32 s4, 0xa37fcc69
	v_cvt_f64_f32_e32 v[0:1], v59
	s_mov_b32 s5, 0x3fee7078
	v_cvt_f64_f32_e32 v[2:3], v57
	s_cmp_eq_u32 s33, 47
	v_fmac_f64_e32 v[0:1], s[4:5], v[44:45]
	v_fmac_f64_e32 v[2:3], s[4:5], v[48:49]
	s_cselect_b64 vcc, -1, 0
	s_cmp_eq_u32 s33, 15
	v_cndmask_b32_e32 v39, v39, v3, vcc
	v_cndmask_b32_e32 v38, v38, v2, vcc
	v_cndmask_b32_e32 v37, v37, v1, vcc
	v_cndmask_b32_e32 v36, v36, v0, vcc
	s_cselect_b64 vcc, -1, 0
	v_cndmask_b32_e32 v5, v5, v3, vcc
	v_cndmask_b32_e32 v4, v4, v2, vcc
	v_cndmask_b32_e32 v7, v7, v1, vcc
	v_cndmask_b32_e32 v6, v6, v0, vcc

	.amdhsa_kernel _Z10snn_kernel6Params
		.amdhsa_group_segment_fixed_size 159008
		.amdhsa_private_segment_fixed_size 0
		.amdhsa_kernarg_size 360
		.amdhsa_user_sgpr_count 2
		.amdhsa_user_sgpr_dispatch_ptr 0
		.amdhsa_user_sgpr_queue_ptr 0
		.amdhsa_user_sgpr_kernarg_segment_ptr 1
		.amdhsa_user_sgpr_dispatch_id 0
		.amdhsa_user_sgpr_kernarg_preload_length 0
		.amdhsa_user_sgpr_kernarg_preload_offset 0
		.amdhsa_user_sgpr_private_segment_size 0
		.amdhsa_uses_dynamic_stack 0
		.amdhsa_enable_private_segment 0
		.amdhsa_system_sgpr_workgroup_id_x 1
		.amdhsa_system_sgpr_workgroup_id_y 0
		.amdhsa_system_sgpr_workgroup_id_z 0
		.amdhsa_system_sgpr_workgroup_info 0
		.amdhsa_system_vgpr_workitem_id 2
		.amdhsa_next_free_vgpr 254
		.amdhsa_next_free_sgpr 96
		.amdhsa_accum_offset 256
		.amdhsa_reserve_vcc 1
		.amdhsa_float_round_mode_32 0
		.amdhsa_float_round_mode_16_64 0
		.amdhsa_float_denorm_mode_32 3
		.amdhsa_float_denorm_mode_16_64 3
		.amdhsa_dx10_clamp 1
		.amdhsa_ieee_mode 1
		.amdhsa_fp16_overflow 0
		.amdhsa_tg_split 0
		.amdhsa_exception_fp_ieee_invalid_op 0
		.amdhsa_exception_fp_denorm_src 0
		.amdhsa_exception_fp_ieee_div_zero 0
		.amdhsa_exception_fp_ieee_overflow 0
		.amdhsa_exception_fp_ieee_underflow 0
		.amdhsa_exception_fp_ieee_inexact 0
		.amdhsa_exception_int_div_zero 0
	.end_amdhsa_kernel

amdhsa.kernels:
  - .agpr_count:     0
    .args:
      - .offset:         0
        .size:           104
        .value_kind:     by_value
      - .offset:         104
        .size:           4
        .value_kind:     hidden_block_count_x
      - .offset:         108
        .size:           4
        .value_kind:     hidden_block_count_y
      - .offset:         112
        .size:           4
        .value_kind:     hidden_block_count_z
      - .offset:         116
        .size:           2
        .value_kind:     hidden_group_size_x
      - .offset:         118
        .size:           2
        .value_kind:     hidden_group_size_y
      - .offset:         120
        .size:           2
        .value_kind:     hidden_group_size_z
      - .offset:         122
        .size:           2
        .value_kind:     hidden_remainder_x
      - .offset:         124
        .size:           2
        .value_kind:     hidden_remainder_y
      - .offset:         126
        .size:           2
        .value_kind:     hidden_remainder_z
      - .offset:         144
        .size:           8
        .value_kind:     hidden_global_offset_x
      - .offset:         152
        .size:           8
        .value_kind:     hidden_global_offset_y
      - .offset:         160
        .size:           8
        .value_kind:     hidden_global_offset_z
      - .offset:         168
        .size:           2
        .value_kind:     hidden_grid_dims
    .group_segment_fixed_size: 159008
    .kernarg_segment_align: 8
    .kernarg_segment_size: 360
    .language:       OpenCL C
    .language_version:
      - 2
      - 0
    .max_flat_workgroup_size: 512
    .name:           _Z10snn_kernel6Params
    .private_segment_fixed_size: 0
    .sgpr_count:     88
    .sgpr_spill_count: 0
    .symbol:         _Z10snn_kernel6Params.kd
    .uniform_work_group_size: 1
    .uses_dynamic_stack: false
    .vgpr_count:     254
    .vgpr_spill_count: 0
    .wavefront_size: 64
